# baseline (speedup 1.0000x reference)
.Lco_nopoll:
	s_waitcnt lgkmcnt(0)
	s_barrier
	v_mov_b32_e32 v76, 0
	v_mov_b32_e32 v77, 0
	v_mov_b32_e32 v78, 0
	v_mov_b32_e32 v79, 0
	ds_write_b128 v74, v[76:79] offset:49152
	ds_write_b128 v74, v[76:79] offset:57344
	v_mov_b32_e32 v0, 0x26400
	v_lshl_add_u32 v0, v75, 5, v0
	ds_read_b128 v[36:39], v0
	ds_read_b128 v[40:43], v0 offset:16
	s_waitcnt lgkmcnt(0)
	v_or3_b32 v44, v36, v37, v38
	v_or3_b32 v44, v44, v39, v40
	v_or3_b32 v44, v44, v41, v42
	v_or_b32_e32 v44, v44, v43
	v_bfe_u32 v44, v44, 15, 1
	v_and_b32_e32 v36, 0x7f, v36
	v_and_b32_e32 v37, 0x7f, v37
	v_and_b32_e32 v38, 0x7f, v38
	v_and_b32_e32 v39, 0x7f, v39
	v_and_b32_e32 v40, 0x7f, v40
	v_and_b32_e32 v41, 0x7f, v41
	v_and_b32_e32 v42, 0x7f, v42
	v_and_b32_e32 v43, 0x7f, v43
	v_mov_b32_e32 v45, v36
	v_add_u32_e32 v46, v45, v37
	v_add_u32_e32 v47, v46, v38
	v_add_u32_e32 v48, v47, v39
	v_add_u32_e32 v49, v48, v40
	v_add_u32_e32 v50, v49, v41
	v_add_u32_e32 v51, v50, v42
	v_add_u32_e32 v52, v51, v43
	v_cmp_lt_u32_e32 vcc, 0x100, v52
	v_add_u32_e32 v53, 15, v52
	v_lshrrev_b32_e32 v53, 4, v53
	v_cndmask_b32_e64 v54, 0, 1, vcc
	v_or_b32_e32 v44, v44, v54
	v_mov_b32_e32 v55, 0x26c00
	v_cmp_eq_u32_e32 vcc, 0, v70
	s_and_saveexec_b64 s[14:15], vcc
	ds_max_u32 v55, v53
	ds_or_b32 v55, v44 offset:4
	s_mov_b64 exec, s[14:15]
	s_waitcnt lgkmcnt(0)
	s_barrier
	ds_read_b64 v[0:1], v55
	v_lshlrev_b32_e32 v56, 5, v45
	v_lshlrev_b32_e32 v57, 5, v46
	v_lshlrev_b32_e32 v58, 5, v47
	v_lshlrev_b32_e32 v59, 5, v48
	v_lshlrev_b32_e32 v60, 5, v49
	v_lshlrev_b32_e32 v61, 5, v50
	v_lshlrev_b32_e32 v62, 5, v51
	v_sub_u32_e32 v56, 0x800, v56
	v_sub_u32_e32 v57, 0x1000, v57
	v_sub_u32_e32 v58, 0x1800, v58
	v_sub_u32_e32 v59, 0x2000, v59
	v_sub_u32_e32 v60, 0x2800, v60
	v_sub_u32_e32 v61, 0x3000, v61
	v_sub_u32_e32 v62, 0x3800, v62
	v_add_u32_e32 v63, s3, v75
	v_lshlrev_b32_e32 v63, 14, v63
	v_add_u32_e32 v63, 0x800000, v63
	s_waitcnt lgkmcnt(0)
	v_readfirstlane_b32 s77, v0
	v_readfirstlane_b32 s36, v1
	s_add_i32 s77, s77, 0
	s_cmp_lg_u32 s36, 0
	s_cselect_b64 s[6:7], 0, -1
	s_cmp_gt_u32 s10, 3
	s_cbranch_scc1 .Lco_done
	s_cmp_lg_u32 s36, 0
	s_cbranch_scc1 .Lco_gen
	s_mov_b32 s89, 0
